# v24 + rows1m: gate-bias table load issued before the router-weight LDS staging loop instead of serialised in front of the barrier
# baseline (speedup 1.0000x reference)
.LBB0_1187:
	s_mov_b32 s3, s84
	v_mov_b32_e32 v44, v194
	v_readlane_b32 s12, v254, 36
	v_readlane_b32 s13, v254, 37
	s_nop 0
	v_add_u32_e32 v46, s12, v44
	v_cmp_gt_i32_e64 s[38:39], 32, v46
	v_lshl_add_u32 v49, v46, 2, 0
	s_and_saveexec_b64 s[24:25], s[38:39]
	ds_write_b32 v49, v187 offset:256
	s_or_b64 exec, exec, s[24:25]
	v_readlane_b32 s12, v253, 32
	v_readlane_b32 s13, v253, 33
	s_mov_b32 s13, s97
	v_writelane_b32 v253, s12, 32
	s_movk_i32 s2, 0x2040
	v_cmp_gt_i32_e32 vcc, s2, v46
	v_writelane_b32 v253, s13, 33
	s_lshl_b32 s40, s12, 6
	s_mov_b32 s41, s97
	s_lshl_b64 s[40:41], s[40:41], 2
	s_add_u32 s40, s76, s40
	s_addc_u32 s41, s77, s41
	s_add_u32 s40, s40, 0x4fc0000
	s_addc_u32 s41, s41, 0
	v_mov_b32_e32 v100, v46
	v_ashrrev_i32_e32 v101, 31, v46
	v_lshl_add_u64 v[100:101], v[100:101], 2, s[40:41]
	v_cmp_gt_i32_e64 s[24:25], 64, v46
	s_nop 1
	s_and_saveexec_b64 s[40:41], s[24:25]
	s_cbranch_execz .Lr1m_gbskip
	global_load_dword v100, v[100:101], off
.Lr1m_gbskip:
	s_mov_b64 exec, s[40:41]
	s_and_saveexec_b64 s[80:81], vcc
	s_cbranch_execz .LBB0_1224
	v_readlane_b32 s12, v253, 32
	s_mul_hi_u32 s2, s12, 0x20400
	s_mul_i32 s12, s12, 0x20400
	v_readlane_b32 s13, v253, 33
	s_add_u32 s12, s14, s12
	s_addc_u32 s13, s15, s2
	v_readlane_b32 s14, v254, 36
	v_ashrrev_i32_e32 v45, 31, v44
	v_readlane_b32 s15, v254, 37
	v_readlane_b32 s2, v254, 35
	s_mov_b64 s[78:79], 0
	v_lshl_add_u64 v[2:3], s[14:15], 0, v[44:45]
	v_lshl_add_u64 v[2:3], v[2:3], 4, s[12:13]
	s_mov_b64 s[12:13], 0x4f10000
	v_lshl_add_u32 v1, v44, 4, s2
	v_lshl_add_u64 v[38:39], v[2:3], 0, s[12:13]
	v_mov_b32_e32 v40, v46
	s_branch .LBB0_1192

.LBB0_1224:
	s_or_b64 exec, exec, s[80:81]
	v_cmp_gt_i32_e32 vcc, 64, v46
	s_and_saveexec_b64 s[14:15], vcc
	s_cbranch_execz .LBB0_1226
	s_waitcnt vmcnt(0)
	ds_write_b32 v49, v100 offset:1024
